# P8/P9 prologue de-serialisation: tile-count word and the six tile->expert words requested together (clamp applied afterwards by scalar select) instead of two dependent round trips
# speedup vs baseline: 1.0195x; 1.0006x over previous
.LBB0_797:
	s_mov_b32 s98, s30
	s_and_b32 s99, s30, 7
	s_lshl_b32 s99, s99, 5
	s_lshr_b32 s30, s30, 3
	s_or_b32 s30, s30, s99
	s_lshl_b32 s99, s30, 3
	s_nop 0
	v_writelane_b32 v253, s99, 19
	s_cmp_lt_i32 s90, 9
	s_cselect_b64 s[0:1], -1, 0
	s_and_b64 s[2:3], s[0:1], s[2:3]
	s_andn2_b64 vcc, exec, s[2:3]
	s_cbranch_vccnz .LBB0_863
	v_mov_b32_e32 v0, 0x780000
	global_load_dword v0, v0, s[88:89] offset:1200 sc1
	s_add_u32 s4, s88, 0x7804b0
	s_addc_u32 s5, s89, 0
	s_add_i32 s8, s76, s30
	s_add_i32 s10, s8, s76
	s_add_i32 s12, s10, s76
	s_add_i32 s14, s12, s76
	s_add_i32 s16, s14, s76
	s_ashr_i32 s70, s30, 2
	s_ashr_i32 s9, s8, 2
	s_ashr_i32 s11, s10, 2
	s_ashr_i32 s13, s12, 2
	s_ashr_i32 s15, s14, 2
	s_ashr_i32 s17, s16, 2
	v_mov_b32_e32 v193, 0
	s_lshl_b32 s2, s70, 2
	s_add_u32 s2, s6, s2
	s_addc_u32 s3, s7, 0
	global_load_dword v1, v193, s[2:3] sc1
	s_lshl_b32 s2, s9, 2
	s_add_u32 s2, s6, s2
	s_addc_u32 s3, s7, 0
	global_load_dword v2, v193, s[2:3] sc1
	s_lshl_b32 s2, s11, 2
	s_add_u32 s2, s6, s2
	s_addc_u32 s3, s7, 0
	global_load_dword v3, v193, s[2:3] sc1
	s_lshl_b32 s2, s13, 2
	s_add_u32 s2, s6, s2
	s_addc_u32 s3, s7, 0
	global_load_dword v4, v193, s[2:3] sc1
	s_lshl_b32 s2, s15, 2
	s_add_u32 s2, s6, s2
	s_addc_u32 s3, s7, 0
	global_load_dword v5, v193, s[2:3] sc1
	s_lshl_b32 s2, s17, 2
	s_add_u32 s2, s6, s2
	s_addc_u32 s3, s7, 0
	global_load_dword v17, v193, s[2:3] sc1
	global_load_dword v18, v193, s[6:7] sc1
	v_lshlrev_b32_e32 v6, 4, v236
	v_and_b32_e32 v7, 32, v236
	v_lshrrev_b32_e32 v10, 1, v236
	v_lshlrev_b32_e32 v11, 6, v236
	v_lshlrev_b32_e32 v12, 2, v236
	v_lshrrev_b32_e32 v13, 5, v236
	v_bfe_u32 v14, v236, 2, 2
	v_bitop3_b32 v7, v6, v7, 48 bitop3:0x6c
	v_add_u32_e32 v6, 0x2000, v6
	v_and_b32_e32 v239, 24, v10
	v_and_b32_e32 v10, 0x3c0, v11
	v_and_b32_e32 v11, 32, v12
	v_and_b32_e32 v12, 4, v13
	v_bfe_u32 v8, v236, 2, 4
	v_lshrrev_b32_e32 v9, 3, v236
	v_and_or_b32 v243, v236, 64, v7
	v_lshrrev_b32_e32 v6, 7, v6
	v_lshlrev_b32_e32 v241, 1, v239
	v_or3_b32 v7, v12, v14, v239
	v_and_b32_e32 v238, 15, v236
	v_bitop3_b32 v240, v241, v11, v10 bitop3:0x36
	s_movk_i32 s50, 0x70
	s_movk_i32 s51, 0xf0
	s_movk_i32 s52, 0xe0
	s_movk_i32 s53, 0x60
	v_and_or_b32 v242, v9, s50, v8
	v_and_or_b32 v244, v6, s51, v8
	v_and_or_b32 v245, v6, s52, v7
	v_and_or_b32 v246, v9, s53, v7
	s_waitcnt vmcnt(0)
	v_readfirstlane_b32 s3, v0
	s_lshl_b32 s31, s3, 2
	v_readfirstlane_b32 s3, v18
	v_readfirstlane_b32 s33, v2
	s_cmp_lt_i32 s8, s31
	s_cselect_b32 s33, s33, s3
	v_readfirstlane_b32 s50, v3
	s_cmp_lt_i32 s10, s31
	s_cselect_b32 s50, s50, s3
	v_readfirstlane_b32 s51, v4
	s_cmp_lt_i32 s12, s31
	s_cselect_b32 s51, s51, s3
	v_readfirstlane_b32 s52, v5
	s_cmp_lt_i32 s14, s31
	s_cselect_b32 s52, s52, s3
	v_readfirstlane_b32 s53, v17
	s_cmp_lt_i32 s16, s31
	s_cselect_b32 s53, s53, s3
	v_readfirstlane_b32 s10, v1
	s_cmp_lt_i32 s30, s31
	s_cselect_b32 s10, s10, s3
	s_cmp_ge_i32 s30, s31
	v_readfirstlane_b32 s2, v236
	s_cbranch_scc1 .LBB0_844
	s_add_u32 s8, s88, 0x7a0000
	s_addc_u32 s9, s89, 0
	s_lshl_b32 s3, s70, 8
	s_or_b32 s11, s3, 0x80
	v_or_b32_e32 v6, s3, v242
	v_add_u32_e32 v0, s11, v244
	v_or_b32_e32 v2, s11, v242
	v_or_b32_e32 v4, s3, v244
	v_ashrrev_i32_e32 v7, 31, v6
	v_ashrrev_i32_e32 v1, 31, v0
	v_ashrrev_i32_e32 v3, 31, v2
	v_ashrrev_i32_e32 v5, 31, v4
	v_lshl_add_u64 v[6:7], v[6:7], 2, s[8:9]
	v_lshl_add_u64 v[0:1], v[0:1], 2, s[8:9]
	v_lshl_add_u64 v[2:3], v[2:3], 2, s[8:9]
	v_lshl_add_u64 v[4:5], v[4:5], 2, s[8:9]
	global_load_dword v8, v[6:7], off
	global_load_dword v9, v[4:5], off
	global_load_dword v10, v[2:3], off
	global_load_dword v11, v[0:1], off
	s_and_b32 s11, s30, 3
	s_lshl_b32 s10, s10, 2
	s_or_b32 s44, s10, s11
	s_lshr_b32 s18, s2, 6
	s_ashr_i32 s45, s44, 31
	s_lshr_b32 s3, s2, 8
	s_lshl_b32 s54, s18, 10
	s_lshl_b64 s[10:11], s[44:45], 19
	s_add_u32 s20, s86, s10
	s_addc_u32 s21, s87, s11
	s_add_i32 s45, s54, 0
	v_lshl_or_b32 v192, v246, 11, v243
	s_add_i32 m0, s45, 0x10000
	v_lshl_or_b32 v194, v245, 11, v243
	global_load_lds_dwordx4 v192, s[20:21]
	s_add_i32 m0, s45, 0x12000
	s_add_u32 s10, s20, 0x40000
	global_load_lds_dwordx4 v194, s[20:21]
	s_addc_u32 s11, s21, 0
	s_add_i32 m0, s45, 0x14000
	s_add_i32 s55, s45, 0x2000
	global_load_lds_dwordx4 v192, s[10:11]
	s_add_i32 m0, s45, 0x16000
	s_add_i32 s56, s45, 0x4000
	global_load_lds_dwordx4 v194, s[10:11]
	s_mov_b32 m0, s45
	s_add_i32 s57, s45, 0x6000
	v_mov_b32_e32 v195, v193
	s_cmp_eq_u32 s3, 1
	v_lshl_add_u64 v[6:7], s[20:21], 0, v[192:193]
	v_lshl_add_u64 v[4:5], s[20:21], 0, v[194:195]
	v_mov_b32_e32 v199, v193
	s_cselect_b64 s[10:11], -1, 0
	s_cmp_lg_u32 s3, 1
	v_mov_b32_e32 v3, v193
	s_waitcnt vmcnt(0)
	v_lshl_or_b32 v198, v8, 11, v243
	v_lshl_or_b32 v2, v9, 11, v243
	global_load_lds_dwordx4 v198, s[40:41]
	s_mov_b32 m0, s55
	v_lshl_or_b32 v196, v10, 11, v243
	global_load_lds_dwordx4 v2, s[40:41]
	s_mov_b32 m0, s56
	v_lshl_or_b32 v0, v11, 11, v243
	global_load_lds_dwordx4 v196, s[40:41]
	s_mov_b32 m0, s57
	s_nop 0
	global_load_lds_dwordx4 v0, s[40:41]
	s_cbranch_scc1 .LBB0_801
	s_barrier

.LBB0_917:
	s_cmp_lt_i32 s90, 10
	s_cselect_b64 s[0:1], -1, 0
	s_and_b64 s[2:3], s[0:1], s[2:3]
	s_andn2_b64 vcc, exec, s[2:3]
	s_cbranch_vccnz .LBB0_959
	v_mov_b32_e32 v0, 0x780000
	global_load_dword v0, v0, s[88:89] offset:1200 sc1
	s_add_u32 s2, s88, 0x7804b0
	s_addc_u32 s3, s89, 0
	s_add_i32 s8, s76, s30
	s_add_i32 s10, s8, s76
	s_add_i32 s12, s10, s76
	s_add_i32 s14, s12, s76
	s_add_i32 s16, s14, s76
	s_ashr_i32 s36, s30, 2
	s_ashr_i32 s9, s8, 2
	s_ashr_i32 s11, s10, 2
	s_ashr_i32 s13, s12, 2
	s_ashr_i32 s15, s14, 2
	s_ashr_i32 s17, s16, 2
	v_mov_b32_e32 v129, 0
	s_lshl_b32 s4, s36, 2
	s_add_u32 s4, s6, s4
	s_addc_u32 s5, s7, 0
	global_load_dword v1, v129, s[4:5] sc1
	s_lshl_b32 s4, s9, 2
	s_add_u32 s4, s6, s4
	s_addc_u32 s5, s7, 0
	global_load_dword v2, v129, s[4:5] sc1
	s_lshl_b32 s4, s11, 2
	s_add_u32 s4, s6, s4
	s_addc_u32 s5, s7, 0
	global_load_dword v3, v129, s[4:5] sc1
	s_lshl_b32 s4, s13, 2
	s_add_u32 s4, s6, s4
	s_addc_u32 s5, s7, 0
	global_load_dword v4, v129, s[4:5] sc1
	s_lshl_b32 s4, s15, 2
	s_add_u32 s4, s6, s4
	s_addc_u32 s5, s7, 0
	global_load_dword v5, v129, s[4:5] sc1
	s_lshl_b32 s4, s17, 2
	s_add_u32 s4, s6, s4
	s_addc_u32 s5, s7, 0
	global_load_dword v17, v129, s[4:5] sc1
	global_load_dword v18, v129, s[6:7] sc1
	v_lshrrev_b32_e32 v6, 1, v236
	v_lshrrev_b32_e32 v11, 5, v236
	v_lshlrev_b32_e32 v13, 4, v236
	v_lshlrev_b32_e32 v7, 6, v236
	v_lshlrev_b32_e32 v10, 2, v236
	v_bfe_u32 v12, v236, 2, 2
	v_and_b32_e32 v14, 32, v236
	v_and_b32_e32 v153, 24, v6
	v_and_b32_e32 v16, 4, v11
	v_add_u32_e32 v11, 0x2000, v13
	v_and_b32_e32 v8, 64, v236
	v_bfe_u32 v9, v236, 2, 4
	v_lshrrev_b32_e32 v15, 3, v236
	v_and_b32_e32 v6, 0x3c0, v7
	v_and_b32_e32 v7, 32, v10
	v_bitop3_b32 v10, v13, v14, 48 bitop3:0x6c
	v_lshlrev_b32_e32 v154, 1, v153
	v_or3_b32 v12, v16, v12, v153
	v_lshrrev_b32_e32 v13, 7, v11
	v_and_b32_e32 v152, 15, v236
	v_or_b32_e32 v157, v10, v8
	v_bitop3_b32 v155, v154, v7, v6 bitop3:0x36
	s_movk_i32 s44, 0xe0
	s_movk_i32 s45, 0xf0
	s_movk_i32 s46, 0x60
	s_movk_i32 s47, 0x70
	v_and_or_b32 v156, v15, s47, v9
	v_and_or_b32 v158, v13, s44, v12
	v_and_or_b32 v159, v13, s45, v9
	v_and_or_b32 v160, v15, s46, v12
	s_waitcnt vmcnt(0)
	v_readfirstlane_b32 s5, v0
	s_lshl_b32 s31, s5, 2
	v_readfirstlane_b32 s5, v18
	v_readfirstlane_b32 s33, v2
	s_cmp_lt_i32 s8, s31
	s_cselect_b32 s33, s33, s5
	v_readfirstlane_b32 s44, v3
	s_cmp_lt_i32 s10, s31
	s_cselect_b32 s44, s44, s5
	v_readfirstlane_b32 s45, v4
	s_cmp_lt_i32 s12, s31
	s_cselect_b32 s45, s45, s5
	v_readfirstlane_b32 s46, v5
	s_cmp_lt_i32 s14, s31
	s_cselect_b32 s46, s46, s5
	v_readfirstlane_b32 s47, v17
	s_cmp_lt_i32 s16, s31
	s_cselect_b32 s47, s47, s5
	v_readfirstlane_b32 s4, v1
	s_cmp_lt_i32 s30, s31
	s_cselect_b32 s4, s4, s5
	s_cmp_ge_i32 s30, s31
	v_readfirstlane_b32 s16, v236
	s_cbranch_scc1 .LBB0_950
	s_add_u32 s48, s88, 0x2400000
	s_addc_u32 s49, s89, 0
	s_add_u32 s50, s86, 0x4000000
	s_addc_u32 s51, s87, 0
	s_ashr_i32 s37, s36, 31
	s_and_b32 s5, s30, 3
	s_lshl_b64 s[8:9], s[36:37], 18
	s_add_u32 s20, s48, s8
	s_addc_u32 s21, s49, s9
	s_lshr_b32 s18, s16, 6
	s_lshl_b32 s4, s4, 2
	s_lshr_b32 s17, s16, 8
	s_lshl_b32 s37, s18, 10
	s_or_b32 s38, s4, s5
	s_add_u32 s4, s20, 0x20000
	s_addc_u32 s5, s21, 0
	s_ashr_i32 s39, s38, 31
	s_lshl_b64 s[8:9], s[38:39], 18
	s_add_u32 s34, s50, s8
	s_addc_u32 s35, s51, s9
	s_add_i32 s39, s37, 0
	v_lshl_or_b32 v128, v160, 10, v157
	s_add_i32 m0, s39, 0x10000
	v_lshl_or_b32 v130, v158, 10, v157
	global_load_lds_dwordx4 v128, s[34:35]
	s_add_i32 m0, s39, 0x12000
	s_add_u32 s8, s34, 0x20000
	global_load_lds_dwordx4 v130, s[34:35]
	s_addc_u32 s9, s35, 0
	s_add_i32 m0, s39, 0x14000
	v_lshl_or_b32 v134, v156, 10, v157
	global_load_lds_dwordx4 v128, s[8:9]
	s_add_i32 m0, s39, 0x16000
	s_add_i32 s52, s39, 0x2000
	global_load_lds_dwordx4 v130, s[8:9]
	s_mov_b32 m0, s39
	v_lshl_or_b32 v132, v159, 10, v157
	global_load_lds_dwordx4 v134, s[20:21]
	s_mov_b32 m0, s52
	s_add_i32 s53, s39, 0x4000
	global_load_lds_dwordx4 v132, s[20:21]
	s_mov_b32 m0, s53
	s_add_i32 s54, s39, 0x6000
	global_load_lds_dwordx4 v134, s[4:5]
	s_mov_b32 m0, s54
	v_mov_b32_e32 v131, v129
	global_load_lds_dwordx4 v132, s[4:5]
	v_mov_b32_e32 v135, v129
	v_mov_b32_e32 v133, v129
	s_cmp_eq_u32 s17, 1
	v_lshl_add_u64 v[4:5], s[20:21], 0, v[134:135]
	v_lshl_add_u64 v[6:7], s[20:21], 0, v[132:133]
	v_lshl_add_u64 v[0:1], s[34:35], 0, v[128:129]
	s_cselect_b64 s[4:5], -1, 0
	s_cmp_lg_u32 s17, 1
	v_lshl_add_u64 v[2:3], s[34:35], 0, v[130:131]
	s_cbranch_scc1 .LBB0_921
	s_barrier
